# window and cmp phases: static s_setprio 1 for waves 4-7 (one wave of each SIMD pair) so the pair's MFMA and VALU stretches overlap; the per-PV setprio pairs removed
# speedup vs baseline: 1.0019x; 1.0019x over previous
; #define GAS __attribute__((address_space(1)))
; #define DUPBAR() do { PHASE_BEGIN(); xcd_barrier(bar, F.tid); } while (0)
; #define SEAM(k) do { PHASE_BEGIN(); if (IN(k) && (k) + 1 < hi && (((MK_MASK) >> ((k) + 1)) != 0)) xcd_barrier(bar, F.tid); } while (0)
; __device__ __forceinline__ void vt8_transpose(Frame& F) {
;     ...
;     const int gw = F.vcu * NWAVES + F.wave, NGW = F.G * NWAVES;
;     for (int blk = gw; blk < 2048; blk += NGW) {
;         const GAS unsigned* src = (const GAS unsigned*)(VSu + (size_t)blk * 64 * 64) + F.lane;
; __global__ void __launch_bounds__(NTHR, 2) mega_fwd(Args args) {
;     ...
;     if (IN(11)) { vt8_transpose(F); __syncthreads(); window_phase(F); if (DUP(11)) { DUPBAR(); window_phase(F); } } SEAM(11);
.LBB0_1423:
	s_cmp_lt_i32 s92, 12
	s_cselect_b64 s[2:3], -1, 0
	s_cmp_gt_i32 s93, 11
	s_cselect_b64 s[4:5], -1, 0
	s_and_b64 s[8:9], s[2:3], s[4:5]
	s_andn2_b64 vcc, exec, s[8:9]
	s_cbranch_vccnz .LBB0_1495
	v_readlane_b32 s100, v238, 2
	s_bitcmp1_b32 s100, 8
	s_cbranch_scc0 .Lprio11_lo
	s_setprio 1
.Lprio11_lo:
	s_lshl_b32 s2, s77, 3
	s_add_i32 s4, s2, s96
	s_cmpk_gt_i32 s4, 0x7ff
	s_cbranch_scc1 .LBB0_1427
	v_lshlrev_b32_e32 v0, 1, v32
	s_waitcnt vmcnt(0)
	v_ashrrev_i32_e32 v1, 31, v0
	s_ashr_i32 s5, s4, 31
	s_lshl_b32 s6, s33, 3
	v_lshlrev_b64 v[0:1], 6, v[0:1]
	s_lshl_b64 s[2:3], s[4:5], 13
	v_ashrrev_i32_e32 v33, 31, v32
	v_lshl_add_u64 v[34:35], s[2:3], 0, v[0:1]
	s_ashr_i32 s7, s6, 31
	s_lshl_b64 s[2:3], s[4:5], 14
	s_lshl_b64 s[10:11], s[6:7], 13
	v_lshl_add_u64 v[36:37], v[32:33], 2, s[2:3]
	s_lshl_b64 s[12:13], s[6:7], 14
	s_mov_b32 s5, 0x28001000
	s_mov_b32 s7, 0x28002000
	s_mov_b32 s14, 0x28003000
	s_brev_b32 s15, 36

; #define SBAR() __builtin_amdgcn_sched_barrier(0)
; __device__ __forceinline__ bf16x8 ppack(const f32x4 a, const f32x4 b) { const u32x4 w = pack8f(a, b); return __builtin_bit_cast(bf16x8, w); }
; #define PV_RD(dt) do { TRRD(r[dt][0], vb, (dt) * 32); TRRD(r[dt][1], vb, (dt) * 32 + 4608); TRRD(r[dt][2], vb, (dt) * 32 + 9216); TRRD(r[dt][3], vb, (dt) * 32 + 9216 + 4608); } while (0)
; #define PV_W(n) asm volatile("s_waitcnt lgkmcnt(" #n ")" ::: "memory"); SBAR()
; template <bool WITH_O, class G> __device__ __forceinline__ void online_smc(f32x4 (&s)[4], G& g, const float ref) {
;     ...
;     float ps = 0.f;
; #pragma unroll
;     for (int T_ = 0; T_ < 4; ++T_)
; #pragma unroll
;         for (int i = 0; i < 4; ++i) { s[T_][i] = __builtin_amdgcn_exp2f(s[T_][i]); ps += s[T_][i]; }
;     g.l += ps;
; template <int NG, class G> __device__ __forceinline__ void pv_tile(G& g0, G& g1, const f32x4 (&s0)[4], const f32x4 (&s1)[4], unsigned vb) {
;     const bf16x8 pa0 = ppack(s0[0], s0[1]), pa1 = ppack(s0[2], s0[3]);
;     bf16x8 pb0 = pa0, pb1 = pa1; if (NG == 2) { pb0 = ppack(s1[0], s1[1]); pb1 = ppack(s1[2], s1[3]); }
;     s16x4 r[8][4];
;     ...
;     PV_RD(0); PV_RD(1); PV_RD(2);
;     __builtin_amdgcn_s_setprio(1);
;     PV_W(8); PV_MM(0); SBAR(); PV_RD(3);
;     PV_W(8); PV_MM(1); SBAR(); PV_RD(4);
;     PV_W(8); PV_MM(2); SBAR(); PV_RD(5);
;     PV_W(8); PV_MM(3); SBAR(); PV_RD(6);
;     PV_W(8); PV_MM(4); SBAR(); PV_RD(7);
;     PV_W(8); PV_MM(5); PV_W(4); PV_MM(6); PV_W(0); PV_MM(7);
;     __builtin_amdgcn_s_setprio(0);
;     ...
; }
.LBB0_1468:
	v_exp_f32_e32 v32, v62
	v_exp_f32_e32 v33, v63
	v_exp_f32_e32 v34, v60
	v_exp_f32_e32 v35, v61
	v_add_f32_e32 v36, 0, v32
	v_exp_f32_e32 v37, v58
	v_add_f32_e32 v36, v33, v36
	v_exp_f32_e32 v38, v59
	v_add_f32_e32 v36, v34, v36
	v_exp_f32_e32 v39, v56
	v_add_f32_e32 v36, v35, v36
	v_exp_f32_e32 v40, v57
	v_add_f32_e32 v36, v37, v36
	v_exp_f32_e32 v41, v54
	v_add_f32_e32 v36, v38, v36
	v_exp_f32_e32 v42, v55
	v_add_f32_e32 v36, v39, v36
	v_exp_f32_e32 v43, v52
	v_add_f32_e32 v36, v40, v36
	v_exp_f32_e32 v52, v53
	v_add_f32_e32 v36, v41, v36
	v_exp_f32_e32 v48, v48
	v_add_f32_e32 v36, v42, v36
	v_exp_f32_e32 v49, v49
	v_add_f32_e32 v36, v43, v36
	v_exp_f32_e32 v50, v50
	v_add_f32_e32 v36, v52, v36
	v_exp_f32_e32 v51, v51
	v_add_f32_e32 v36, v48, v36
	v_exp_f32_e32 v16, v16
	v_add_f32_e32 v36, v49, v36
	v_exp_f32_e32 v17, v17
	v_add_f32_e32 v36, v50, v36
	v_exp_f32_e32 v18, v18
	v_add_f32_e32 v36, v51, v36
	v_exp_f32_e32 v19, v19
	v_add_f32_e32 v152, v72, v36
	v_add_f32_e32 v36, 0, v16
	v_exp_f32_e32 v20, v20
	v_add_f32_e32 v36, v17, v36
	v_exp_f32_e32 v21, v21
	v_add_f32_e32 v36, v18, v36
	v_exp_f32_e32 v22, v22
	v_add_f32_e32 v36, v19, v36
	v_exp_f32_e32 v23, v23
	v_add_f32_e32 v36, v20, v36
	v_exp_f32_e32 v24, v24
	v_add_f32_e32 v36, v21, v36
	v_exp_f32_e32 v25, v25
	v_add_f32_e32 v36, v22, v36
	v_exp_f32_e32 v26, v26
	v_add_f32_e32 v36, v23, v36
	v_exp_f32_e32 v27, v27
	v_add_f32_e32 v36, v24, v36
	v_exp_f32_e32 v28, v28
	v_exp_f32_e32 v29, v29
	v_exp_f32_e32 v30, v30
	v_exp_f32_e32 v31, v31
	v_cvt_pk_bf16_f32 v44, v32, v33
	v_cvt_pk_bf16_f32 v45, v34, v35
	v_cvt_pk_bf16_f32 v46, v37, v38
	v_cvt_pk_bf16_f32 v47, v39, v40
	v_cvt_pk_bf16_f32 v80, v41, v42
	v_cvt_pk_bf16_f32 v81, v43, v52
	v_cvt_pk_bf16_f32 v82, v48, v49
	v_cvt_pk_bf16_f32 v83, v50, v51
	v_cvt_pk_bf16_f32 v84, v16, v17
	v_cvt_pk_bf16_f32 v85, v18, v19
	v_cvt_pk_bf16_f32 v86, v20, v21
	v_cvt_pk_bf16_f32 v87, v22, v23
	v_cvt_pk_bf16_f32 v92, v24, v25
	v_cvt_pk_bf16_f32 v93, v26, v27
	v_cvt_pk_bf16_f32 v94, v28, v29
	v_cvt_pk_bf16_f32 v95, v30, v31
	ds_read_b64_tr_b16 v[16:17], v144 offset:0
	v_add_f32_e32 v36, v25, v36
	ds_read_b64_tr_b16 v[18:19], v144 offset:0x1200
	v_add_f32_e32 v36, v26, v36
	ds_read_b64_tr_b16 v[20:21], v144 offset:0x2400
	v_add_f32_e32 v36, v27, v36
	ds_read_b64_tr_b16 v[22:23], v144 offset:0x3600
	v_add_f32_e32 v36, v28, v36
	ds_read_b64_tr_b16 v[24:25], v144 offset:32
	v_add_f32_e32 v36, v29, v36
	ds_read_b64_tr_b16 v[26:27], v144 offset:0x1220
	v_add_f32_e32 v36, v30, v36
	ds_read_b64_tr_b16 v[28:29], v144 offset:0x2420
	v_add_f32_e32 v36, v31, v36
	ds_read_b64_tr_b16 v[30:31], v144 offset:0x3620
	ds_read_b64_tr_b16 v[32:33], v144 offset:64
	ds_read_b64_tr_b16 v[34:35], v144 offset:0x1240
	v_add_f32_e32 v153, v88, v36
	ds_read_b64_tr_b16 v[36:37], v144 offset:0x2440
	ds_read_b64_tr_b16 v[38:39], v144 offset:0x3640
	v_mov_b32_e32 v73, v72
	v_mov_b32_e32 v74, v72
	v_mov_b32_e32 v75, v72
	v_mov_b32_e32 v89, v88
	v_mov_b32_e32 v90, v88
	v_mov_b32_e32 v91, v88
	s_waitcnt lgkmcnt(8)
	v_mfma_f32_16x16x32_bf16 v[40:43], v[16:19], v[44:47], v[72:75]
	v_mfma_f32_16x16x32_bf16 v[16:19], v[16:19], v[84:87], v[88:91]
	v_mfma_f32_16x16x32_bf16 v[48:51], v[20:23], v[80:83], v[40:43]
	v_mfma_f32_16x16x32_bf16 v[16:19], v[20:23], v[92:95], v[16:19]
	ds_read_b64_tr_b16 v[40:41], v144 offset:0x60
	ds_read_b64_tr_b16 v[42:43], v144 offset:0x1260
	ds_read_b64_tr_b16 v[64:65], v144 offset:0x2460
	ds_read_b64_tr_b16 v[66:67], v144 offset:0x3660
	s_waitcnt lgkmcnt(8)
	v_mfma_f32_16x16x32_bf16 v[20:23], v[24:27], v[44:47], v[72:75]
	v_mfma_f32_16x16x32_bf16 v[52:55], v[28:31], v[80:83], v[20:23]
	v_mfma_f32_16x16x32_bf16 v[20:23], v[24:27], v[84:87], v[88:91]
	v_mfma_f32_16x16x32_bf16 v[20:23], v[28:31], v[92:95], v[20:23]
	ds_read_b64_tr_b16 v[76:77], v144 offset:0x80
	ds_read_b64_tr_b16 v[78:79], v144 offset:0x1280
	ds_read_b64_tr_b16 v[98:99], v144 offset:0x2480
	ds_read_b64_tr_b16 v[100:101], v144 offset:0x3680
	s_waitcnt lgkmcnt(8)
	v_mfma_f32_16x16x32_bf16 v[24:27], v[32:35], v[44:47], v[72:75]
	v_mfma_f32_16x16x32_bf16 v[56:59], v[36:39], v[80:83], v[24:27]
	v_mfma_f32_16x16x32_bf16 v[24:27], v[32:35], v[84:87], v[88:91]
	v_mfma_f32_16x16x32_bf16 v[24:27], v[36:39], v[92:95], v[24:27]
	ds_read_b64_tr_b16 v[36:37], v144 offset:0xa0
	ds_read_b64_tr_b16 v[38:39], v144 offset:0x12a0
	ds_read_b64_tr_b16 v[102:103], v144 offset:0x24a0
	ds_read_b64_tr_b16 v[104:105], v144 offset:0x36a0
	s_waitcnt lgkmcnt(8)
	v_mfma_f32_16x16x32_bf16 v[28:31], v[40:43], v[44:47], v[72:75]
	v_mfma_f32_16x16x32_bf16 v[60:63], v[64:67], v[80:83], v[28:31]
	v_mfma_f32_16x16x32_bf16 v[28:31], v[40:43], v[84:87], v[88:91]
	v_mfma_f32_16x16x32_bf16 v[28:31], v[64:67], v[92:95], v[28:31]
	ds_read_b64_tr_b16 v[40:41], v144 offset:0xc0
	ds_read_b64_tr_b16 v[42:43], v144 offset:0x12c0
	ds_read_b64_tr_b16 v[106:107], v144 offset:0x24c0
	ds_read_b64_tr_b16 v[108:109], v144 offset:0x36c0
	s_waitcnt lgkmcnt(8)
	v_mfma_f32_16x16x32_bf16 v[32:35], v[76:79], v[44:47], v[72:75]
	v_mfma_f32_16x16x32_bf16 v[68:71], v[98:101], v[80:83], v[32:35]
	v_mfma_f32_16x16x32_bf16 v[32:35], v[76:79], v[84:87], v[88:91]
	v_mfma_f32_16x16x32_bf16 v[32:35], v[98:101], v[92:95], v[32:35]
	ds_read_b64_tr_b16 v[98:99], v144 offset:0xe0
	ds_read_b64_tr_b16 v[100:101], v144 offset:0x12e0
	ds_read_b64_tr_b16 v[154:155], v144 offset:0x24e0
	ds_read_b64_tr_b16 v[156:157], v144 offset:0x36e0
	s_waitcnt lgkmcnt(8)
	v_mfma_f32_16x16x32_bf16 v[64:67], v[36:39], v[44:47], v[72:75]
	s_waitcnt lgkmcnt(4)
	v_mfma_f32_16x16x32_bf16 v[36:39], v[36:39], v[84:87], v[88:91]
	v_mfma_f32_16x16x32_bf16 v[76:79], v[102:105], v[80:83], v[64:67]
	v_mfma_f32_16x16x32_bf16 v[36:39], v[102:105], v[92:95], v[36:39]
	v_mfma_f32_16x16x32_bf16 v[64:67], v[40:43], v[44:47], v[72:75]
	s_waitcnt lgkmcnt(0)
	v_mfma_f32_16x16x32_bf16 v[40:43], v[40:43], v[84:87], v[88:91]
	v_mfma_f32_16x16x32_bf16 v[64:67], v[106:109], v[80:83], v[64:67]
	v_mfma_f32_16x16x32_bf16 v[40:43], v[106:109], v[92:95], v[40:43]
	v_mfma_f32_16x16x32_bf16 v[44:47], v[98:101], v[44:47], v[72:75]
	v_mfma_f32_16x16x32_bf16 v[72:75], v[154:157], v[80:83], v[44:47]
	v_mfma_f32_16x16x32_bf16 v[44:47], v[98:101], v[84:87], v[88:91]
	v_mfma_f32_16x16x32_bf16 v[44:47], v[154:157], v[92:95], v[44:47]
	v_cmp_eq_u32_e32 vcc, s36, v96
	s_cbranch_vccnz .LBB0_1437
	s_and_b32 s5, s43, 0x3fc0
	s_min_u32 s5, s5, 0x200
	v_or_b32_e32 v80, s5, v140
	v_sub_u32_e32 v154, v115, v80
	v_add_u32_e32 v155, s5, v117
	v_add_u32_e32 v156, s5, v145
	s_sub_i32 s5, 0, s52
	s_mov_b32 s36, 1
	s_mov_b32 s37, -2
	s_branch .LBB0_1471
; #define SBAR() __builtin_amdgcn_sched_barrier(0)
; __device__ __forceinline__ bf16x8 ppack(const f32x4 a, const f32x4 b) { const u32x4 w = pack8f(a, b); return __builtin_bit_cast(bf16x8, w); }
; #define PV_RD(dt) do { TRRD(r[dt][0], vb, (dt) * 32); TRRD(r[dt][1], vb, (dt) * 32 + 4608); TRRD(r[dt][2], vb, (dt) * 32 + 9216); TRRD(r[dt][3], vb, (dt) * 32 + 9216 + 4608); } while (0)
; #define PV_W(n) asm volatile("s_waitcnt lgkmcnt(" #n ")" ::: "memory"); SBAR()
; template <bool WITH_O, class G> __device__ __forceinline__ void online_smc(f32x4 (&s)[4], G& g, const float ref) {
;     ...
;     float ps = 0.f;
; #pragma unroll
;     for (int T_ = 0; T_ < 4; ++T_)
; #pragma unroll
;         for (int i = 0; i < 4; ++i) { s[T_][i] = __builtin_amdgcn_exp2f(s[T_][i]); ps += s[T_][i]; }
;     g.l += ps;
; template <int NG, class G> __device__ __forceinline__ void pv_tile(G& g0, G& g1, const f32x4 (&s0)[4], const f32x4 (&s1)[4], unsigned vb) {
;     const bf16x8 pa0 = ppack(s0[0], s0[1]), pa1 = ppack(s0[2], s0[3]);
;     bf16x8 pb0 = pa0, pb1 = pa1; if (NG == 2) { pb0 = ppack(s1[0], s1[1]); pb1 = ppack(s1[2], s1[3]); }
;     s16x4 r[8][4];
;     ...
;     PV_RD(0); PV_RD(1); PV_RD(2);
;     __builtin_amdgcn_s_setprio(1);
;     PV_W(8); PV_MM(0); SBAR(); PV_RD(3);
;     PV_W(8); PV_MM(1); SBAR(); PV_RD(4);
;     PV_W(8); PV_MM(2); SBAR(); PV_RD(5);
;     PV_W(8); PV_MM(3); SBAR(); PV_RD(6);
;     PV_W(8); PV_MM(4); SBAR(); PV_RD(7);
;     PV_W(8); PV_MM(5); PV_W(4); PV_MM(6); PV_W(0); PV_MM(7);
;     __builtin_amdgcn_s_setprio(0);
;     ...
; }
.LBB0_1470:
	v_exp_f32_e32 v100, v100
	v_exp_f32_e32 v101, v101
	v_exp_f32_e32 v102, v102
	v_exp_f32_e32 v103, v103
	v_add_f32_e32 v130, 0, v100
	v_exp_f32_e32 v108, v108
	v_add_f32_e32 v130, v101, v130
	v_exp_f32_e32 v109, v109
	v_add_f32_e32 v130, v102, v130
	v_exp_f32_e32 v110, v110
	v_add_f32_e32 v130, v103, v130
	v_exp_f32_e32 v111, v111
	v_add_f32_e32 v130, v108, v130
	v_exp_f32_e32 v104, v104
	v_add_f32_e32 v130, v109, v130
	v_exp_f32_e32 v105, v105
	v_add_f32_e32 v130, v110, v130
	v_exp_f32_e32 v106, v106
	v_add_f32_e32 v130, v111, v130
	v_exp_f32_e32 v107, v107
	v_add_f32_e32 v130, v104, v130
	v_exp_f32_e32 v96, v96
	v_add_f32_e32 v130, v105, v130
	v_exp_f32_e32 v97, v97
	v_add_f32_e32 v130, v106, v130
	v_exp_f32_e32 v98, v98
	v_add_f32_e32 v130, v107, v130
	v_exp_f32_e32 v99, v99
	v_add_f32_e32 v130, v96, v130
	v_exp_f32_e32 v92, v92
	v_add_f32_e32 v130, v97, v130
	v_exp_f32_e32 v93, v93
	v_add_f32_e32 v130, v98, v130
	v_exp_f32_e32 v94, v94
	v_add_f32_e32 v130, v99, v130
	v_exp_f32_e32 v95, v95
	v_add_f32_e32 v152, v152, v130
	v_add_f32_e32 v130, 0, v92
	v_exp_f32_e32 v134, v88
	v_add_f32_e32 v130, v93, v130
	v_exp_f32_e32 v136, v89
	v_add_f32_e32 v130, v94, v130
	v_exp_f32_e32 v138, v90
	v_add_f32_e32 v130, v95, v130
	v_exp_f32_e32 v91, v91
	v_add_f32_e32 v88, v134, v130
	v_exp_f32_e32 v130, v80
	v_add_f32_e32 v88, v136, v88
	v_exp_f32_e32 v139, v81
	v_add_f32_e32 v88, v138, v88
	v_exp_f32_e32 v157, v82
	v_add_f32_e32 v88, v91, v88
	v_exp_f32_e32 v158, v83
	v_add_f32_e32 v80, v130, v88
	v_exp_f32_e32 v159, v84
	v_add_f32_e32 v80, v139, v80
	v_exp_f32_e32 v160, v85
	v_add_f32_e32 v80, v157, v80
	v_exp_f32_e32 v161, v86
	v_add_f32_e32 v80, v158, v80
	v_exp_f32_e32 v162, v87
	v_add_f32_e32 v80, v159, v80
	v_add_f32_e32 v80, v160, v80
	v_add_f32_e32 v80, v161, v80
	v_add_f32_e32 v80, v162, v80
	s_addk_i32 s6, 0x2400
	v_add_f32_e32 v153, v153, v80
	v_add_u32_e32 v166, s6, v142
	v_cvt_pk_bf16_f32 v80, v100, v101
	v_cvt_pk_bf16_f32 v81, v102, v103
	v_cvt_pk_bf16_f32 v82, v108, v109
	v_cvt_pk_bf16_f32 v83, v110, v111
	v_cvt_pk_bf16_f32 v84, v104, v105
	v_cvt_pk_bf16_f32 v85, v106, v107
	v_cvt_pk_bf16_f32 v86, v96, v97
	v_cvt_pk_bf16_f32 v87, v98, v99
	v_cvt_pk_bf16_f32 v88, v92, v93
	v_cvt_pk_bf16_f32 v89, v94, v95
	v_cvt_pk_bf16_f32 v90, v134, v136
	v_cvt_pk_bf16_f32 v91, v138, v91
	v_cvt_pk_bf16_f32 v92, v130, v139
	v_cvt_pk_bf16_f32 v93, v157, v158
	v_cvt_pk_bf16_f32 v94, v159, v160
	v_cvt_pk_bf16_f32 v95, v161, v162
	ds_read_b64_tr_b16 v[96:97], v166 offset:0
	ds_read_b64_tr_b16 v[98:99], v166 offset:0x1200
	ds_read_b64_tr_b16 v[100:101], v166 offset:0x2400
	ds_read_b64_tr_b16 v[102:103], v166 offset:0x3600
	ds_read_b64_tr_b16 v[104:105], v166 offset:32
	ds_read_b64_tr_b16 v[106:107], v166 offset:0x1220
	ds_read_b64_tr_b16 v[108:109], v166 offset:0x2420
	ds_read_b64_tr_b16 v[110:111], v166 offset:0x3620
	ds_read_b64_tr_b16 v[158:159], v166 offset:64
	ds_read_b64_tr_b16 v[160:161], v166 offset:0x1240
	ds_read_b64_tr_b16 v[162:163], v166 offset:0x2440
	ds_read_b64_tr_b16 v[164:165], v166 offset:0x3640
	s_waitcnt lgkmcnt(8)
	v_mfma_f32_16x16x32_bf16 v[48:51], v[96:99], v[80:83], v[48:51]
	v_mfma_f32_16x16x32_bf16 v[16:19], v[96:99], v[88:91], v[16:19]
	v_mfma_f32_16x16x32_bf16 v[48:51], v[100:103], v[84:87], v[48:51]
	v_mfma_f32_16x16x32_bf16 v[16:19], v[100:103], v[92:95], v[16:19]
	ds_read_b64_tr_b16 v[96:97], v166 offset:0x60
	ds_read_b64_tr_b16 v[98:99], v166 offset:0x1260
	ds_read_b64_tr_b16 v[100:101], v166 offset:0x2460
	ds_read_b64_tr_b16 v[102:103], v166 offset:0x3660
	s_waitcnt lgkmcnt(8)
	v_mfma_f32_16x16x32_bf16 v[52:55], v[104:107], v[80:83], v[52:55]
	v_mfma_f32_16x16x32_bf16 v[20:23], v[104:107], v[88:91], v[20:23]
	v_mfma_f32_16x16x32_bf16 v[52:55], v[108:111], v[84:87], v[52:55]
	v_mfma_f32_16x16x32_bf16 v[20:23], v[108:111], v[92:95], v[20:23]
	ds_read_b64_tr_b16 v[104:105], v166 offset:0x80
	ds_read_b64_tr_b16 v[106:107], v166 offset:0x1280
	ds_read_b64_tr_b16 v[108:109], v166 offset:0x2480
	ds_read_b64_tr_b16 v[110:111], v166 offset:0x3680
	s_waitcnt lgkmcnt(8)
	v_mfma_f32_16x16x32_bf16 v[56:59], v[158:161], v[80:83], v[56:59]
	v_mfma_f32_16x16x32_bf16 v[24:27], v[158:161], v[88:91], v[24:27]
	v_mfma_f32_16x16x32_bf16 v[56:59], v[162:165], v[84:87], v[56:59]
	v_mfma_f32_16x16x32_bf16 v[24:27], v[162:165], v[92:95], v[24:27]
	ds_read_b64_tr_b16 v[158:159], v166 offset:0xa0
	ds_read_b64_tr_b16 v[160:161], v166 offset:0x12a0
	ds_read_b64_tr_b16 v[162:163], v166 offset:0x24a0
	ds_read_b64_tr_b16 v[164:165], v166 offset:0x36a0
	s_waitcnt lgkmcnt(8)
	v_mfma_f32_16x16x32_bf16 v[60:63], v[96:99], v[80:83], v[60:63]
	v_mfma_f32_16x16x32_bf16 v[28:31], v[96:99], v[88:91], v[28:31]
	v_mfma_f32_16x16x32_bf16 v[60:63], v[100:103], v[84:87], v[60:63]
	v_mfma_f32_16x16x32_bf16 v[28:31], v[100:103], v[92:95], v[28:31]
	ds_read_b64_tr_b16 v[96:97], v166 offset:0xc0
	ds_read_b64_tr_b16 v[98:99], v166 offset:0x12c0
	ds_read_b64_tr_b16 v[100:101], v166 offset:0x24c0
	ds_read_b64_tr_b16 v[102:103], v166 offset:0x36c0
	s_waitcnt lgkmcnt(8)
	v_mfma_f32_16x16x32_bf16 v[68:71], v[104:107], v[80:83], v[68:71]
	v_mfma_f32_16x16x32_bf16 v[32:35], v[104:107], v[88:91], v[32:35]
	v_mfma_f32_16x16x32_bf16 v[68:71], v[108:111], v[84:87], v[68:71]
	v_mfma_f32_16x16x32_bf16 v[32:35], v[108:111], v[92:95], v[32:35]
	ds_read_b64_tr_b16 v[104:105], v166 offset:0xe0
	ds_read_b64_tr_b16 v[106:107], v166 offset:0x12e0
	ds_read_b64_tr_b16 v[108:109], v166 offset:0x24e0
	ds_read_b64_tr_b16 v[110:111], v166 offset:0x36e0
	s_waitcnt lgkmcnt(8)
	v_mfma_f32_16x16x32_bf16 v[76:79], v[158:161], v[80:83], v[76:79]
	s_waitcnt lgkmcnt(4)
	v_mfma_f32_16x16x32_bf16 v[36:39], v[158:161], v[88:91], v[36:39]
	v_mfma_f32_16x16x32_bf16 v[76:79], v[162:165], v[84:87], v[76:79]
	v_mfma_f32_16x16x32_bf16 v[36:39], v[162:165], v[92:95], v[36:39]
	v_mfma_f32_16x16x32_bf16 v[64:67], v[96:99], v[80:83], v[64:67]
	s_waitcnt lgkmcnt(0)
	v_mfma_f32_16x16x32_bf16 v[40:43], v[96:99], v[88:91], v[40:43]
	v_mfma_f32_16x16x32_bf16 v[64:67], v[100:103], v[84:87], v[64:67]
	v_mfma_f32_16x16x32_bf16 v[40:43], v[100:103], v[92:95], v[40:43]
	v_mfma_f32_16x16x32_bf16 v[72:75], v[104:107], v[80:83], v[72:75]
	v_mfma_f32_16x16x32_bf16 v[44:47], v[104:107], v[88:91], v[44:47]
	v_mfma_f32_16x16x32_bf16 v[72:75], v[108:111], v[84:87], v[72:75]
	v_mfma_f32_16x16x32_bf16 v[44:47], v[108:111], v[92:95], v[44:47]
	s_add_i32 s36, s36, 1
	s_add_i32 s37, s37, -1
	s_add_i32 s6, s5, s36
	v_add_u32_e32 v154, 64, v154
	v_subrev_u32_e32 v155, 64, v155
	s_cmp_eq_u32 s6, 1
	v_subrev_u32_e32 v156, 64, v156
	s_cbranch_scc1 .LBB0_1437

; __device__ __forceinline__ void xcd_barrier(const XcdBarrier& b, int tid) {
;     asm volatile("s_waitcnt vmcnt(0)" ::: "memory");
;     __syncthreads();
;     if (tid == 0) {
;         unsigned* bar = b.bar;
;         __builtin_amdgcn_s_waitcnt(0);
;         unsigned nloc = b.st[0], nx = b.st[1];
;         if (nloc == 0u) { xcd_barrier_complete(bar, b.x, nloc, nx); b.st[0] = nloc; b.st[1] = nx; }
.LBB0_1495:
	s_setprio 0
	s_cmp_gt_i32 s93, 12
	s_cselect_b64 s[2:3], -1, 0
	s_and_b64 s[4:5], s[8:9], s[2:3]
	s_andn2_b64 vcc, exec, s[4:5]
	v_readlane_b32 s4, v238, 2
	v_mbcnt_lo_u32_b32 v143, -1, 0
	v_mbcnt_hi_u32_b32 v143, -1, v143
	s_nop 1
	v_add_u32_e32 v112, s4, v143
	s_cbranch_vccnz .LBB0_1549
	s_waitcnt vmcnt(0)
	v_cmp_eq_u32_e32 vcc, 0, v112
	s_waitcnt vmcnt(0) lgkmcnt(0)
	s_barrier
	s_and_saveexec_b64 s[4:5], vcc
	s_cbranch_execz .LBB0_1548
	s_add_i32 s6, 0, 0x23c00
	v_mov_b32_e32 v0, s6
	s_waitcnt vmcnt(0) expcnt(0) lgkmcnt(0)
	ds_read_b32 v2, v0
	s_add_i32 s6, 0, 0x23c04
	v_mov_b32_e32 v0, s6
	ds_read_b32 v0, v0
	s_waitcnt lgkmcnt(1)
	v_cmp_ne_u32_e32 vcc, 0, v2
	s_cbranch_vccnz .LBB0_1512
	v_readlane_b32 s6, v238, 0
	v_readlane_b32 s7, v238, 1
	s_load_dwordx2 s[10:11], s[6:7], 0x4
	s_add_u32 s6, s26, 0x1000
	s_addc_u32 s7, s27, 0
	s_add_u32 s8, s26, 0x1100
	s_addc_u32 s9, s27, 0
	s_waitcnt lgkmcnt(0)
	s_mul_i32 s22, s10, s33
	s_add_u32 s10, s26, 0x1200
	s_mul_i32 s22, s22, s11
	s_addc_u32 s11, s27, 0
	s_add_u32 s12, s26, 0x1300
	s_addc_u32 s13, s27, 0
	s_mov_b32 s23, 1
	v_mov_b32_e32 v16, 0
	s_branch .LBB0_1500

; #define LAS __attribute__((address_space(3)))
; __device__ __forceinline__ void ring8_lane_init(Ring8Lane& R, int wave, int lane) {
; #pragma unroll
;     for (int k = 0; k < 4; ++k) { const int n = wave + 8 * k; int row, ch; unsigned off;
;         if (n < 9) { const int o = n * 1024 + lane * 16; row = o / K8ST; ch = (o % K8ST) >> 4; if (ch > 7) ch = 7; if (row > 63) row = 63; off = (unsigned)(row * 128 + ch * 16); }
;         else { const int o = (n - 9) * 1024 + lane * 16; row = o / VST; ch = (o % VST) >> 4; if (ch > 15) ch = 15; if (row > 63) row = 63; off = (unsigned)(row * 256 + ch * 16); }
;         R.so[k] = off; }
; }
; __device__ __forceinline__ void cmp_phase(Frame& F) {
;     const bf16* Q = (const bf16*)(F.ws + SC_Q); const char* KC = (const char*)(F.ws + SC_KC); const char* VC = KC + (size_t)8 * 1024 * HD * 2;
;     bf16* OC = (bf16*)(F.ws + SC_OW); const float* gates = (const float*)(F.ws + SM_GATES); unsigned long long* SELM = (unsigned long long*)(F.ws + SM_SELM);
;     const int lane = F.lane, c = lane & 15, kq = lane >> 4;
;     LAS float* imp = (LAS float*)(F.lds + IMP_OFF); LAS unsigned long long* Ml = (LAS unsigned long long*)(F.lds + SELM_OFF);
;     const unsigned vlane = (unsigned)((4 * kq + (c >> 2)) * VST + 8 * (c & 3)); const int klane = c * K8ST + 32 * kq;
;     Ring8Lane RL; ring8_lane_init(RL, F.wave, lane);
.LBB0_1549:
	s_cmp_lt_i32 s92, 13
	s_cselect_b64 s[4:5], -1, 0
	s_and_b64 s[42:43], s[4:5], s[2:3]
	s_andn2_b64 vcc, exec, s[42:43]
	s_cbranch_vccnz .LBB0_1636
	v_readlane_b32 s100, v238, 2
	s_bitcmp1_b32 s100, 8
	s_cbranch_scc0 .Lprio12_lo
	s_setprio 1
.Lprio12_lo:
	s_waitcnt vmcnt(0)
	v_lshlrev_b32_e32 v2, 4, v143
	s_lshl_b32 s16, s96, 10
	s_cmpk_gt_u32 s21, 0x23f
	v_add_u32_e32 v0, 0xffffdc00, v2
	s_cbranch_scc0 .LBB0_1552
	v_add_u32_e32 v3, s16, v0
	s_mov_b32 s2, 0x38e38e39
	v_mul_hi_i32 v1, v3, s2
	v_lshrrev_b32_e32 v4, 31, v1
	v_ashrrev_i32_e32 v1, 6, v1
	v_add_u32_e32 v1, v1, v4
	v_mul_i32_i24_e32 v4, 0x120, v1
	v_sub_u32_e32 v3, v3, v4
	v_ashrrev_i32_e32 v3, 4, v3
	v_min_i32_e32 v3, 15, v3
	s_mov_b32 s4, 8
	s_cbranch_execz .LBB0_1553
	s_branch .LBB0_1554

; #define LAS __attribute__((address_space(3)))
; __device__ __forceinline__ unsigned lds_addr(const LAS void* p) { return (unsigned)(size_t)p; }
; __device__ __forceinline__ void imp_accum(const f32x4 (&s)[4], float& carry, LAS float* impt  , int jb, int c, int q4, int lane) {
;     float rot[4];
; #pragma unroll
;     for (int T_ = 0; T_ < 4; ++T_) rot[T_] = __shfl(s[T_][3], (lane + 48) & 63);
; #pragma unroll
;     for (int T_ = 0; T_ < 4; ++T_) { const float prev = (q4 == 0) ? (T_ == 0 ? carry : rot[T_ == 0 ? 0 : T_ - 1]) : rot[T_];
;         float v = (s[T_][0] + s[T_][1]) + (s[T_][2] + s[T_][3]) + prev;
;         v += __builtin_bit_cast(float, __builtin_amdgcn_mov_dpp(__builtin_bit_cast(int, v), 0xB1, 0xF, 0xF, true));
;         v += __builtin_bit_cast(float, __builtin_amdgcn_mov_dpp(__builtin_bit_cast(int, v), 0x4E, 0xF, 0xF, true));
;         if ((c & 3) == 0) impt[jb + 4 * T_ + q4] = v; }
;     carry = rot[3];
; }
; __device__ __forceinline__ void cmp_phase(Frame& F) {
;     ...
;                     for (int q = 0; q < 4; ++q) { s0[T_][q] = __builtin_amdgcn_exp2f(s0[T_][q]); s1[T_][q] = __builtin_amdgcn_exp2f(s1[T_][q]); }
;                 imp_accum(s0, carry0, impA, kt * 16, c, kq, lane); imp_accum(s1, carry1, impB, kt * 16, c, kq, lane);
;                 pv_tile<2>(g0, g1, s0, s1, lds_addr(sb + K8TB) + vlane);
.LBB0_1585:
	s_and_b64 vcc, exec, s[22:23]
	s_cbranch_vccz .LBB0_1570
	v_exp_f32_e32 v138, v109
	v_exp_f32_e32 v109, v110
	v_exp_f32_e32 v110, v111
	v_exp_f32_e32 v134, v108
	v_exp_f32_e32 v108, v107
	v_exp_f32_e32 v107, v103
	v_exp_f32_e32 v103, v99
	ds_bpermute_b32 v146, v183, v110
	ds_bpermute_b32 v145, v183, v108
	ds_bpermute_b32 v144, v183, v107
	ds_bpermute_b32 v99, v183, v103
	v_add_f32_e32 v147, v134, v138
	v_add_f32_e32 v148, v109, v110
	s_waitcnt lgkmcnt(0)
	v_cndmask_b32_e64 v196, v146, v193, s[2:3]
	v_add_f32_e32 v147, v147, v148
	v_add_f32_e32 v196, v147, v196
	s_add_i32 s22, s79, s48
	v_add_u32_e32 v111, s22, v117
	v_exp_f32_e32 v140, v104
	v_exp_f32_e32 v105, v105
	v_exp_f32_e32 v104, v106
	v_cndmask_b32_e64 v197, v145, v146, s[2:3]
	v_add_f32_e32 v146, v140, v105
	v_add_f32_e32 v147, v104, v108
	v_add_f32_e32 v146, v146, v147
	v_add_f32_e32 v197, v146, v197
	v_exp_f32_e32 v106, v100
	v_exp_f32_e32 v101, v101
	v_exp_f32_e32 v100, v102
	v_cndmask_b32_e64 v198, v144, v145, s[2:3]
	v_add_f32_e32 v145, v106, v101
	v_add_f32_e32 v146, v100, v107
	v_add_f32_e32 v145, v145, v146
	v_add_f32_e32 v198, v145, v198
	v_exp_f32_e32 v102, v96
	v_exp_f32_e32 v97, v97
	v_exp_f32_e32 v96, v98
	v_cndmask_b32_e64 v199, v99, v144, s[2:3]
	v_add_f32_e32 v144, v102, v97
	v_add_f32_e32 v145, v96, v103
	v_add_f32_e32 v144, v144, v145
	v_add_f32_e32 v199, v144, v199
	v_exp_f32_e32 v91, v91
	v_exp_f32_e32 v98, v88
	v_exp_f32_e32 v144, v89
	v_exp_f32_e32 v89, v87
	v_exp_f32_e32 v88, v83
	v_exp_f32_e32 v87, v95
	ds_bpermute_b32 v147, v183, v91
	v_exp_f32_e32 v90, v90
	ds_bpermute_b32 v146, v183, v89
	ds_bpermute_b32 v145, v183, v88
	ds_bpermute_b32 v83, v183, v87
	v_add_f32_e32 v148, v98, v144
	v_add_f32_e32 v149, v90, v91
	s_waitcnt lgkmcnt(0)
	v_cndmask_b32_e64 v200, v147, v192, s[2:3]
	v_add_f32_e32 v148, v148, v149
	v_add_f32_e32 v200, v148, v200
	v_exp_f32_e32 v95, v84
	v_exp_f32_e32 v85, v85
	v_exp_f32_e32 v84, v86
	v_cndmask_b32_e64 v201, v146, v147, s[2:3]
	v_add_f32_e32 v147, v95, v85
	v_add_f32_e32 v148, v84, v89
	v_add_f32_e32 v147, v147, v148
	v_add_f32_e32 v201, v147, v201
	v_exp_f32_e32 v86, v80
	v_exp_f32_e32 v81, v81
	v_exp_f32_e32 v80, v82
	v_cndmask_b32_e64 v202, v145, v146, s[2:3]
	v_add_f32_e32 v146, v86, v81
	v_add_f32_e32 v147, v80, v88
	v_add_f32_e32 v146, v146, v147
	v_add_f32_e32 v202, v146, v202
	v_exp_f32_e32 v92, v92
	v_exp_f32_e32 v93, v93
	v_exp_f32_e32 v82, v94
	v_cndmask_b32_e64 v203, v83, v145, s[2:3]
	v_add_f32_e32 v145, v92, v93
	v_add_f32_e32 v146, v82, v87
	v_add_f32_e32 v145, v145, v146
	v_add_f32_e32 v203, v145, v203
	v_add_f32_dpp v196, v196, v196 quad_perm:[1,0,3,2] row_mask:0xf bank_mask:0xf bound_ctrl:1
	v_add_f32_dpp v197, v197, v197 quad_perm:[1,0,3,2] row_mask:0xf bank_mask:0xf bound_ctrl:1
	v_add_f32_dpp v198, v198, v198 quad_perm:[1,0,3,2] row_mask:0xf bank_mask:0xf bound_ctrl:1
	v_add_f32_dpp v199, v199, v199 quad_perm:[1,0,3,2] row_mask:0xf bank_mask:0xf bound_ctrl:1
	v_add_f32_dpp v200, v200, v200 quad_perm:[1,0,3,2] row_mask:0xf bank_mask:0xf bound_ctrl:1
	v_add_f32_dpp v201, v201, v201 quad_perm:[1,0,3,2] row_mask:0xf bank_mask:0xf bound_ctrl:1
	v_add_f32_dpp v202, v202, v202 quad_perm:[1,0,3,2] row_mask:0xf bank_mask:0xf bound_ctrl:1
	v_add_f32_dpp v203, v203, v203 quad_perm:[1,0,3,2] row_mask:0xf bank_mask:0xf bound_ctrl:1
	v_mov_b32_dpp v204, v196 quad_perm:[2,3,0,1] row_mask:0xf bank_mask:0xf bound_ctrl:1
	v_mov_b32_dpp v205, v197 quad_perm:[2,3,0,1] row_mask:0xf bank_mask:0xf bound_ctrl:1
	v_mov_b32_dpp v206, v198 quad_perm:[2,3,0,1] row_mask:0xf bank_mask:0xf bound_ctrl:1
	v_mov_b32_dpp v207, v199 quad_perm:[2,3,0,1] row_mask:0xf bank_mask:0xf bound_ctrl:1
	v_mov_b32_dpp v208, v200 quad_perm:[2,3,0,1] row_mask:0xf bank_mask:0xf bound_ctrl:1
	v_mov_b32_dpp v209, v201 quad_perm:[2,3,0,1] row_mask:0xf bank_mask:0xf bound_ctrl:1
	v_mov_b32_dpp v210, v202 quad_perm:[2,3,0,1] row_mask:0xf bank_mask:0xf bound_ctrl:1
	v_mov_b32_dpp v211, v203 quad_perm:[2,3,0,1] row_mask:0xf bank_mask:0xf bound_ctrl:1
	s_and_saveexec_b64 s[22:23], s[4:5]
	v_add_u32_e32 v212, 0x117c1, v111
	v_add_f32_e32 v196, v196, v204
	v_add_f32_e32 v197, v197, v205
	v_add_f32_e32 v198, v198, v206
	v_add_f32_e32 v199, v199, v207
	v_add_f32_e32 v200, v200, v208
	v_add_f32_e32 v201, v201, v209
	v_add_f32_e32 v202, v202, v210
	v_add_f32_e32 v203, v203, v211
	ds_write_b32 v212, v196
	ds_write_b32 v212, v197 offset:16
	ds_write_b32 v212, v198 offset:32
	ds_write_b32 v212, v199 offset:48
	ds_write_b32 v212, v200 offset:4096
	ds_write_b32 v212, v201 offset:4112
	ds_write_b32 v212, v202 offset:4128
	ds_write_b32 v212, v203 offset:4144
	s_or_b64 exec, exec, s[22:23]
	s_addk_i32 s37, 0x2400
	v_add_u32_e32 v145, s37, v173
	v_cvt_pk_bf16_f32 v146, v134, v138
	v_cvt_pk_bf16_f32 v147, v109, v110
	v_cvt_pk_bf16_f32 v148, v140, v105
	v_cvt_pk_bf16_f32 v149, v104, v108
	v_cvt_pk_bf16_f32 v104, v106, v101
	v_cvt_pk_bf16_f32 v105, v100, v107
	v_cvt_pk_bf16_f32 v106, v102, v97
	v_cvt_pk_bf16_f32 v107, v96, v103
	v_cvt_pk_bf16_f32 v100, v98, v144
	v_cvt_pk_bf16_f32 v101, v90, v91
	v_cvt_pk_bf16_f32 v102, v95, v85
	v_cvt_pk_bf16_f32 v103, v84, v89
	v_cvt_pk_bf16_f32 v84, v86, v81
	v_cvt_pk_bf16_f32 v85, v80, v88
	v_cvt_pk_bf16_f32 v86, v92, v93
	v_cvt_pk_bf16_f32 v87, v82, v87
	ds_read_b64_tr_b16 v[88:89], v145 offset:0
	ds_read_b64_tr_b16 v[90:91], v145 offset:0x1200
	ds_read_b64_tr_b16 v[92:93], v145 offset:0x2400
	ds_read_b64_tr_b16 v[94:95], v145 offset:0x3600
	ds_read_b64_tr_b16 v[108:109], v145 offset:32
	ds_read_b64_tr_b16 v[110:111], v145 offset:0x1220
	ds_read_b64_tr_b16 v[150:151], v145 offset:0x2420
	ds_read_b64_tr_b16 v[152:153], v145 offset:0x3620
	ds_read_b64_tr_b16 v[154:155], v145 offset:64
	ds_read_b64_tr_b16 v[156:157], v145 offset:0x1240
	ds_read_b64_tr_b16 v[158:159], v145 offset:0x2440
	ds_read_b64_tr_b16 v[160:161], v145 offset:0x3640
	s_waitcnt lgkmcnt(8)
; #define SBAR() __builtin_amdgcn_sched_barrier(0)
; __device__ __forceinline__ bf16x8 ppack(const f32x4 a, const f32x4 b) { const u32x4 w = pack8f(a, b); return __builtin_bit_cast(bf16x8, w); }
; #define PV_RD(dt) do { TRRD(r[dt][0], vb, (dt) * 32); TRRD(r[dt][1], vb, (dt) * 32 + 4608); TRRD(r[dt][2], vb, (dt) * 32 + 9216); TRRD(r[dt][3], vb, (dt) * 32 + 9216 + 4608); } while (0)
; #define PV_W(n) asm volatile("s_waitcnt lgkmcnt(" #n ")" ::: "memory"); SBAR()
; template <int NG, class G> __device__ __forceinline__ void pv_tile(G& g0, G& g1, const f32x4 (&s0)[4], const f32x4 (&s1)[4], unsigned vb) {
;     const bf16x8 pa0 = ppack(s0[0], s0[1]), pa1 = ppack(s0[2], s0[3]);
;     bf16x8 pb0 = pa0, pb1 = pa1; if (NG == 2) { pb0 = ppack(s1[0], s1[1]); pb1 = ppack(s1[2], s1[3]); }
;     s16x4 r[8][4];
;     ...
;     PV_RD(0); PV_RD(1); PV_RD(2);
;     __builtin_amdgcn_s_setprio(1);
;     PV_W(8); PV_MM(0); SBAR(); PV_RD(3);
;     PV_W(8); PV_MM(1); SBAR(); PV_RD(4);
;     PV_W(8); PV_MM(2); SBAR(); PV_RD(5);
;     PV_W(8); PV_MM(3); SBAR(); PV_RD(6);
;     PV_W(8); PV_MM(4); SBAR(); PV_RD(7);
;     PV_W(8); PV_MM(5); PV_W(4); PV_MM(6); PV_W(0); PV_MM(7);
;     __builtin_amdgcn_s_setprio(0);
;     ...
; }
	v_mfma_f32_16x16x32_bf16 v[76:79], v[88:91], v[146:149], v[76:79]
	v_mfma_f32_16x16x32_bf16 v[44:47], v[88:91], v[100:103], v[44:47]
	v_mfma_f32_16x16x32_bf16 v[76:79], v[92:95], v[104:107], v[76:79]
	v_mfma_f32_16x16x32_bf16 v[44:47], v[92:95], v[84:87], v[44:47]
	ds_read_b64_tr_b16 v[88:89], v145 offset:0x60
	ds_read_b64_tr_b16 v[90:91], v145 offset:0x1260
	ds_read_b64_tr_b16 v[92:93], v145 offset:0x2460
	ds_read_b64_tr_b16 v[94:95], v145 offset:0x3660
	s_waitcnt lgkmcnt(8)
	v_mfma_f32_16x16x32_bf16 v[72:75], v[108:111], v[146:149], v[72:75]
	v_mfma_f32_16x16x32_bf16 v[40:43], v[108:111], v[100:103], v[40:43]
	v_mfma_f32_16x16x32_bf16 v[72:75], v[150:153], v[104:107], v[72:75]
	v_mfma_f32_16x16x32_bf16 v[40:43], v[150:153], v[84:87], v[40:43]
	ds_read_b64_tr_b16 v[108:109], v145 offset:0x80
	ds_read_b64_tr_b16 v[110:111], v145 offset:0x1280
	ds_read_b64_tr_b16 v[150:151], v145 offset:0x2480
	ds_read_b64_tr_b16 v[152:153], v145 offset:0x3680
	s_waitcnt lgkmcnt(8)
	v_mfma_f32_16x16x32_bf16 v[68:71], v[154:157], v[146:149], v[68:71]
	v_mfma_f32_16x16x32_bf16 v[36:39], v[154:157], v[100:103], v[36:39]
	v_mfma_f32_16x16x32_bf16 v[68:71], v[158:161], v[104:107], v[68:71]
	v_mfma_f32_16x16x32_bf16 v[36:39], v[158:161], v[84:87], v[36:39]
	ds_read_b64_tr_b16 v[154:155], v145 offset:0xa0
	ds_read_b64_tr_b16 v[156:157], v145 offset:0x12a0
	ds_read_b64_tr_b16 v[158:159], v145 offset:0x24a0
	ds_read_b64_tr_b16 v[160:161], v145 offset:0x36a0
	s_waitcnt lgkmcnt(8)
	v_mfma_f32_16x16x32_bf16 v[64:67], v[88:91], v[146:149], v[64:67]
	v_mfma_f32_16x16x32_bf16 v[32:35], v[88:91], v[100:103], v[32:35]
	v_mfma_f32_16x16x32_bf16 v[64:67], v[92:95], v[104:107], v[64:67]
	v_mfma_f32_16x16x32_bf16 v[32:35], v[92:95], v[84:87], v[32:35]
	ds_read_b64_tr_b16 v[88:89], v145 offset:0xc0
	ds_read_b64_tr_b16 v[90:91], v145 offset:0x12c0
	ds_read_b64_tr_b16 v[92:93], v145 offset:0x24c0
	ds_read_b64_tr_b16 v[94:95], v145 offset:0x36c0
	s_waitcnt lgkmcnt(8)
	v_mfma_f32_16x16x32_bf16 v[60:63], v[108:111], v[146:149], v[60:63]
	v_mfma_f32_16x16x32_bf16 v[28:31], v[108:111], v[100:103], v[28:31]
	v_mfma_f32_16x16x32_bf16 v[60:63], v[150:153], v[104:107], v[60:63]
	v_mfma_f32_16x16x32_bf16 v[28:31], v[150:153], v[84:87], v[28:31]
	ds_read_b64_tr_b16 v[108:109], v145 offset:0xe0
	ds_read_b64_tr_b16 v[110:111], v145 offset:0x12e0
	ds_read_b64_tr_b16 v[150:151], v145 offset:0x24e0
	ds_read_b64_tr_b16 v[152:153], v145 offset:0x36e0
	s_waitcnt lgkmcnt(8)
	v_mfma_f32_16x16x32_bf16 v[56:59], v[154:157], v[146:149], v[56:59]
	s_waitcnt lgkmcnt(4)
	v_mfma_f32_16x16x32_bf16 v[24:27], v[154:157], v[100:103], v[24:27]
	v_mfma_f32_16x16x32_bf16 v[56:59], v[158:161], v[104:107], v[56:59]
	v_mfma_f32_16x16x32_bf16 v[24:27], v[158:161], v[84:87], v[24:27]
	v_mfma_f32_16x16x32_bf16 v[52:55], v[88:91], v[146:149], v[52:55]
	s_waitcnt lgkmcnt(0)
	v_mfma_f32_16x16x32_bf16 v[20:23], v[88:91], v[100:103], v[20:23]
	v_mfma_f32_16x16x32_bf16 v[52:55], v[92:95], v[104:107], v[52:55]
	v_mfma_f32_16x16x32_bf16 v[20:23], v[92:95], v[84:87], v[20:23]
	v_mfma_f32_16x16x32_bf16 v[48:51], v[108:111], v[146:149], v[48:51]
	v_mfma_f32_16x16x32_bf16 v[16:19], v[108:111], v[100:103], v[16:19]
	v_mfma_f32_16x16x32_bf16 v[48:51], v[150:153], v[104:107], v[48:51]
	v_mfma_f32_16x16x32_bf16 v[16:19], v[150:153], v[84:87], v[16:19]
	v_mov_b32_e32 v192, v83
	v_mov_b32_e32 v193, v99
	s_sub_i32 s59, s59, 64
	s_add_i32 s79, s79, 64
	s_and_b64 vcc, exec, s[54:55]
	s_cbranch_vccz .LBB0_1571

; #define DUPBAR() do { PHASE_BEGIN(); xcd_barrier(bar, F.tid); } while (0)
; #define SEAM(k) do { PHASE_BEGIN(); if (IN(k) && (k) + 1 < hi && (((MK_MASK) >> ((k) + 1)) != 0)) xcd_barrier(bar, F.tid); } while (0)
; __global__ void __launch_bounds__(NTHR, 2) mega_fwd(Args args) {
;     ...
;     if (IN(12)) { cmp_phase(F); if (DUP(12)) { DUPBAR(); cmp_phase(F); } } SEAM(12);
;     if (IN(13)) { if (DUP(13)) { sel_phase<true>(F); DUPBAR(); } sel_phase<false>(F); } SEAM(13);
.LBB0_1636:
	s_setprio 0
	s_cmp_gt_i32 s93, 13
	s_cselect_b64 s[2:3], -1, 0
	s_and_b64 s[4:5], s[42:43], s[2:3]
	s_andn2_b64 vcc, exec, s[4:5]
	v_readlane_b32 s4, v238, 2
	s_waitcnt vmcnt(0)
	v_mbcnt_lo_u32_b32 v2, -1, 0
	v_mbcnt_hi_u32_b32 v2, -1, v2
	s_nop 0
	v_add_u32_e32 v100, s4, v2
	s_branch .LBB0_1690
